# baseline (speedup 1.0000x reference)
amdhsa.kernels:
  - .agpr_count:     0
    .args:
      - .actual_access:  read_only
        .address_space:  global
        .offset:         0
        .size:           8
        .value_kind:     global_buffer
      - .actual_access:  read_only
        .address_space:  global
        .offset:         8
        .size:           8
        .value_kind:     global_buffer
      - .actual_access:  read_only
        .address_space:  global
        .offset:         16
        .size:           8
        .value_kind:     global_buffer
      - .actual_access:  write_only
        .address_space:  global
        .offset:         24
        .size:           8
        .value_kind:     global_buffer
      - .actual_access:  write_only
        .address_space:  global
        .offset:         32
        .size:           8
        .value_kind:     global_buffer
    .group_segment_fixed_size: 0
    .kernarg_segment_align: 8
    .kernarg_segment_size: 40
    .language:       OpenCL C
    .language_version:
      - 2
      - 0
    .max_flat_workgroup_size: 256
    .name:           _Z12wprep_kernelPKfS0_S0_PDF16_Pj
    .private_segment_fixed_size: 0
    .sgpr_count:     18
    .sgpr_spill_count: 0
    .symbol:         _Z12wprep_kernelPKfS0_S0_PDF16_Pj.kd
    .uniform_work_group_size: 1
    .uses_dynamic_stack: false
    .vgpr_count:     12
    .vgpr_spill_count: 0
    .wavefront_size: 64
  - .agpr_count:     0
    .args:
      - .actual_access:  read_only
        .address_space:  global
        .offset:         0
        .size:           8
        .value_kind:     global_buffer
      - .actual_access:  read_only
        .address_space:  global
        .offset:         8
        .size:           8
        .value_kind:     global_buffer
      - .actual_access:  read_only
        .address_space:  global
        .offset:         16
        .size:           8
        .value_kind:     global_buffer
      - .actual_access:  read_only
        .address_space:  global
        .offset:         24
        .size:           8
        .value_kind:     global_buffer
      - .actual_access:  read_only
        .address_space:  global
        .offset:         32
        .size:           8
        .value_kind:     global_buffer
      - .actual_access:  read_only
        .address_space:  global
        .offset:         40
        .size:           8
        .value_kind:     global_buffer
      - .actual_access:  read_only
        .address_space:  global
        .offset:         48
        .size:           8
        .value_kind:     global_buffer
      - .actual_access:  write_only
        .address_space:  global
        .offset:         56
        .size:           8
        .value_kind:     global_buffer
      - .actual_access:  write_only
        .address_space:  global
        .offset:         64
        .size:           8
        .value_kind:     global_buffer
      - .actual_access:  write_only
        .address_space:  global
        .offset:         72
        .size:           8
        .value_kind:     global_buffer
      - .address_space:  global
        .offset:         80
        .size:           8
        .value_kind:     global_buffer
    .group_segment_fixed_size: 0
    .kernarg_segment_align: 8
    .kernarg_segment_size: 88
    .language:       OpenCL C
    .language_version:
      - 2
      - 0
    .max_flat_workgroup_size: 512
    .name:           _Z11proj_kernelPKfS0_S0_PKDF16_S0_S0_S0_PDF16_S3_S3_Pj
    .private_segment_fixed_size: 0
    .sgpr_count:     70
    .sgpr_spill_count: 0
    .symbol:         _Z11proj_kernelPKfS0_S0_PKDF16_S0_S0_S0_PDF16_S3_S3_Pj.kd
    .uniform_work_group_size: 1
    .uses_dynamic_stack: false
    .vgpr_count:     256
    .vgpr_spill_count: 0
    .wavefront_size: 64
  - .agpr_count:     0
    .args:
      - .actual_access:  read_only
        .address_space:  global
        .offset:         0
        .size:           8
        .value_kind:     global_buffer
      - .address_space:  global
        .offset:         8
        .size:           8
        .value_kind:     global_buffer
      - .address_space:  global
        .offset:         16
        .size:           8
        .value_kind:     global_buffer
      - .actual_access:  read_only
        .address_space:  global
        .offset:         24
        .size:           8
        .value_kind:     global_buffer
      - .actual_access:  write_only
        .address_space:  global
        .offset:         32
        .size:           8
        .value_kind:     global_buffer
    .group_segment_fixed_size: 0
    .kernarg_segment_align: 8
    .kernarg_segment_size: 40
    .language:       OpenCL C
    .language_version:
      - 2
      - 0
    .max_flat_workgroup_size: 512
    .name:           _Z11attn_kernelPKDF16_S0_S0_PKjPf
    .private_segment_fixed_size: 0
    .sgpr_count:     43
    .sgpr_spill_count: 0
    .symbol:         _Z11attn_kernelPKDF16_S0_S0_PKjPf.kd
    .uniform_work_group_size: 1
    .uses_dynamic_stack: false
    .vgpr_count:     192
    .vgpr_spill_count: 0
    .wavefront_size: 64
